# guconv: layer-0 down-proj weight conversion moved from the NA background task into the gate/up GEMM unit epilogues (one 16k x 64n group per unit and wave, 16-B stores); NA converts gate/up layer 0 onl
# baseline (speedup 1.0000x reference)
.LBB0_253:
	s_cmp_lt_i32 s30, 4
	s_cselect_b64 s[8:9], -1, 0
	s_and_b64 s[4:5], s[8:9], s[4:5]
	s_andn2_b64 vcc, exec, s[4:5]
	s_cbranch_vccnz .LBB0_364
	s_mov_b64 s[10:11], s[0:1]
	s_mov_b32 s98, 0x18000
	s_cmpk_eq_u32 s22, 0x100
	s_cselect_b32 s98, 0x8000, s98
	s_mov_b32 s99, 0
	s_load_dwordx2 s[4:5], s[10:11], 0xd8
	v_readlane_b32 s12, v255, 6
	s_mul_i32 s6, s12, 0x2080
	v_mbcnt_hi_u32_b32 v4, -1, v208
	s_add_i32 s6, s6, 0
	s_waitcnt lgkmcnt(0)
	s_add_u32 s23, s4, 0x11800000
	v_lshlrev_b32_e32 v2, 2, v4
	v_and_b32_e32 v210, 60, v2
	v_lshlrev_b32_e32 v2, 3, v4
	s_addc_u32 s26, s5, 0
	v_and_b32_e32 v194, 24, v2
	v_ashrrev_i32_e32 v211, 2, v4
	s_add_u32 s27, s4, 0x1800000
	v_ashrrev_i32_e32 v209, 4, v4
	s_movk_i32 s7, 0x104
	v_mul_u32_u24_e32 v2, 0x104, v194
	v_mov_b32_e32 v3, 0
	v_and_b32_e32 v5, -4, v4
	v_add_u32_e32 v213, 16, v211
	v_add_u32_e32 v215, 32, v211
	v_add_u32_e32 v217, 48, v211
	s_addc_u32 s35, s5, 0
	s_mov_b32 s65, 0
	v_lshl_add_u32 v220, v210, 2, s6
	v_mul_lo_u32 v221, v209, s7
	v_mov_b32_e32 v195, v3
	v_add3_u32 v219, s6, v2, v5
	v_ashrrev_i32_e32 v212, 31, v211
	v_ashrrev_i32_e32 v214, 31, v213
	v_ashrrev_i32_e32 v216, 31, v215
	s_cmpk_gt_i32 s88, 0x81f
	v_ashrrev_i32_e32 v218, 31, v217
	s_cbranch_scc1 .LBB0_352
	s_add_u32 s15, s4, 0x25b00000
	s_addc_u32 s48, s5, 0
	s_add_u32 s49, s4, 0x29c00000
	s_addc_u32 s50, s5, 0
	s_add_u32 s51, s4, 0x2dd00000
	s_addc_u32 s53, s5, 0
	v_and_b32_e32 v2, 31, v4
	v_ashrrev_i32_e32 v4, 3, v4
	s_lshl_b32 s54, s12, 5
	s_lshr_b32 s55, s3, 7
	v_and_b32_e32 v222, -4, v4
	v_lshl_add_u64 v[4:5], s[4:5], 0, v[2:3]
	s_mov_b64 s[4:5], 0x31e00000
	v_and_or_b32 v2, s54, 32, v2
	s_cmp_lg_u32 0, -1
	v_lshl_add_u64 v[196:197], v[4:5], 0, s[4:5]
	v_sub_u32_e64 v4, v2, 8 clamp
	s_cselect_b32 s4, 0, 0
	s_and_b32 s3, s3, 0xffffff80
	v_min_u32_e32 v223, 48, v4
	s_sub_i32 s3, s4, s3
	v_sub_u32_e32 v224, 15, v2
	v_add_u32_e32 v225, 16, v223
	s_mov_b32 s13, 0
	s_add_i32 s3, s3, 0x8800
	s_mov_b64 s[20:21], 0
	s_mov_b64 s[18:19], 0
	s_mov_b32 s56, 0x41000000
	s_mov_b32 s14, 0x42000000
	s_movk_i32 s57, 0x1e0
	s_movk_i32 s58, 0xffdf
	s_add_i32 s59, 0, 0x4000
	s_mov_b32 s60, s88
	s_mov_b32 s61, s88
	s_mov_b32 s63, 0
	s_mov_b32 s62, s52
	s_cmpk_gt_i32 s61, 0x7ff
	s_mov_b64 s[4:5], -1
	s_cbranch_scc0 .LBB0_290
	s_branch .LBB0_257

.LBB0_684:
	v_lshrrev_b32_e32 v7, 1, v194
	s_add_u32 s46, s12, 0x3a000000
	v_and_b32_e32 v7, 24, v7
	s_addc_u32 s47, s13, 0
	v_and_b32_e32 v6, 15, v194
	v_lshlrev_b32_e32 v8, 1, v7
	s_add_u32 s48, s40, 0x80
	v_lshl_or_b32 v198, s4, 6, v6
	v_lshl_or_b32 v6, v6, 6, v8
	v_lshlrev_b32_e32 v8, 2, v194
	s_addc_u32 s49, s41, 0
	s_lshl_b32 s4, s4, 13
	v_and_b32_e32 v8, 32, v8
	v_bitop3_b32 v9, v6, s4, v8 bitop3:0xde
	s_lshl_b32 s4, s5, 5
	s_and_b32 s39, s4, 0x60
	s_lshl_b32 s4, s39, 7
	v_bitop3_b32 v6, v6, s4, v8 bitop3:0xde
	s_add_u32 s4, s58, 0x80
	s_waitcnt vmcnt(2)
	s_barrier
	s_addc_u32 s5, s59, 0
	s_add_i32 s76, s35, 0x18000
	s_mov_b32 s51, m0
	s_mov_b32 m0, s76
	s_nop 0
	global_load_lds_dwordx4 v196, s[4:5]
	s_mov_b32 m0, s51
	s_add_i32 s77, s35, 0x1a000
	s_mov_b32 s51, m0
	s_mov_b32 m0, s77
	s_nop 0
	global_load_lds_dwordx4 v197, s[4:5]
	s_mov_b32 m0, s51
	s_add_i32 s78, s35, 0x8000
	s_mov_b32 s4, m0
	s_mov_b32 m0, s78
	s_nop 0
	global_load_lds_dwordx4 v218, s[48:49]
	s_mov_b32 m0, s4
	s_add_i32 s79, s35, 0xa000
	s_mov_b32 s4, m0
	s_mov_b32 m0, s79
	s_nop 0
	global_load_lds_dwordx4 v215, s[48:49]
	s_mov_b32 m0, s4
	s_add_u32 s4, s58, 0x20080
	s_addc_u32 s5, s59, 0
	s_add_i32 s80, s35, 0x1c000
	s_mov_b32 s48, m0
	s_mov_b32 m0, s80
	s_nop 0
	global_load_lds_dwordx4 v196, s[4:5]
	s_mov_b32 m0, s48
	s_add_i32 s81, s35, 0x1e000
	s_mov_b32 s48, m0
	s_mov_b32 m0, s81
	s_nop 0
	global_load_lds_dwordx4 v197, s[4:5]
	s_mov_b32 m0, s48
	s_waitcnt vmcnt(6)
	s_add_i32 s82, s35, 0xc000
	s_cmpk_lt_u32 s17, 0x100
	v_mov_b32_e32 v67, 0
	s_cselect_b64 s[48:49], -1, 0
	v_or_b32_e32 v199, s39, v7
	v_readfirstlane_b32 s89, v0
	v_readfirstlane_b32 s90, v0
	v_mov_b32_e32 v200, s50
	v_mov_b32_e32 v210, s19
	s_mov_b32 s83, 0x20000
	s_mov_b64 s[50:51], 0x1000
	s_movk_i32 s84, 0x1000
	s_mov_b32 s54, 0x3d000000
	s_mov_b32 s85, 0xc0e00000
	s_mov_b32 s56, 0xc01d265f
	s_mov_b32 s86, 0x24000
	s_mov_b32 s87, 0x28000
	v_add_u32_e32 v201, 0, v6
	v_add_u32_e32 v202, 0, v9
	v_mov_b32_e32 v203, 0x40e00000
	v_mov_b32_e32 v66, 0
	v_mov_b32_e32 v68, v67
	v_mov_b32_e32 v69, v67
	v_mov_b32_e32 v70, 0
	v_mov_b32_e32 v71, v67
	v_mov_b32_e32 v72, v67
	v_mov_b32_e32 v73, v67
	v_mov_b32_e32 v74, 0
	v_mov_b32_e32 v75, v67
	v_mov_b32_e32 v76, v67
	v_mov_b32_e32 v77, v67
	v_mov_b32_e32 v78, 0
	v_mov_b32_e32 v79, v67
	v_mov_b32_e32 v80, v67
	v_mov_b32_e32 v81, v67
	v_mov_b32_e32 v82, 0
	v_mov_b32_e32 v83, v67
	v_mov_b32_e32 v84, v67
	v_mov_b32_e32 v85, v67
	v_mov_b32_e32 v86, 0
	v_mov_b32_e32 v87, v67
	v_mov_b32_e32 v88, v67
	v_mov_b32_e32 v89, v67
	v_mov_b32_e32 v90, 0
	v_mov_b32_e32 v91, v67
	v_mov_b32_e32 v92, v67
	v_mov_b32_e32 v93, v67
	v_mov_b32_e32 v94, 0
	v_mov_b32_e32 v95, v67
	v_mov_b32_e32 v96, v67
	v_mov_b32_e32 v97, v67
	v_mov_b32_e32 v98, 0
	v_mov_b32_e32 v99, v67
	v_mov_b32_e32 v100, v67
	v_mov_b32_e32 v101, v67
	v_mov_b32_e32 v102, 0
	v_mov_b32_e32 v103, v67
	v_mov_b32_e32 v104, v67
	v_mov_b32_e32 v105, v67
	v_mov_b32_e32 v106, 0
	v_mov_b32_e32 v107, v67
	v_mov_b32_e32 v108, v67
	v_mov_b32_e32 v109, v67
	v_mov_b32_e32 v110, 0
	v_mov_b32_e32 v111, v67
	v_mov_b32_e32 v112, v67
	v_mov_b32_e32 v113, v67
	v_mov_b32_e32 v114, 0
	v_mov_b32_e32 v115, v67
	v_mov_b32_e32 v116, v67
	v_mov_b32_e32 v117, v67
	v_mov_b32_e32 v118, 0
	v_mov_b32_e32 v119, v67
	v_mov_b32_e32 v120, v67
	v_mov_b32_e32 v121, v67
	v_mov_b32_e32 v122, 0
	v_mov_b32_e32 v123, v67
	v_mov_b32_e32 v124, v67
	v_mov_b32_e32 v125, v67
	v_mov_b32_e32 v126, 0
	v_mov_b32_e32 v127, v67
	v_mov_b32_e32 v128, v67
	v_mov_b32_e32 v129, v67
	s_waitcnt vmcnt(6)
	v_mov_b32_e32 v130, 0
	v_mov_b32_e32 v131, v67
	v_mov_b32_e32 v132, v67
	v_mov_b32_e32 v133, v67
	v_mov_b32_e32 v134, 0
	v_mov_b32_e32 v135, v67
	v_mov_b32_e32 v136, v67
	v_mov_b32_e32 v137, v67
	s_waitcnt vmcnt(4)
	v_mov_b32_e32 v138, 0
	v_mov_b32_e32 v139, v67
	v_mov_b32_e32 v140, v67
	v_mov_b32_e32 v141, v67
	v_mov_b32_e32 v142, 0
	v_mov_b32_e32 v143, v67
	v_mov_b32_e32 v144, v67
	v_mov_b32_e32 v145, v67
	s_waitcnt vmcnt(2)
	v_mov_b32_e32 v146, 0
	v_mov_b32_e32 v147, v67
	v_mov_b32_e32 v148, v67
	v_mov_b32_e32 v149, v67
	v_mov_b32_e32 v150, 0
	v_mov_b32_e32 v151, v67
	v_mov_b32_e32 v152, v67
	v_mov_b32_e32 v153, v67
	s_waitcnt vmcnt(0)
	v_mov_b32_e32 v154, 0
	v_mov_b32_e32 v155, v67
	v_mov_b32_e32 v156, v67
	v_mov_b32_e32 v157, v67
	v_mov_b32_e32 v158, 0
	v_mov_b32_e32 v159, v67
	v_mov_b32_e32 v160, v67
	v_mov_b32_e32 v161, v67
	v_mov_b32_e32 v162, 0
	v_mov_b32_e32 v163, v67
	v_mov_b32_e32 v164, v67
	v_mov_b32_e32 v165, v67
	v_mov_b32_e32 v166, 0
	v_mov_b32_e32 v167, v67
	v_mov_b32_e32 v168, v67
	v_mov_b32_e32 v169, v67
	v_mov_b32_e32 v170, 0
	v_mov_b32_e32 v171, v67
	v_mov_b32_e32 v172, v67
	v_mov_b32_e32 v173, v67
	v_mov_b32_e32 v174, 0
	v_mov_b32_e32 v175, v67
	v_mov_b32_e32 v176, v67
	v_mov_b32_e32 v177, v67
	v_mov_b32_e32 v178, 0
	v_mov_b32_e32 v179, v67
	v_mov_b32_e32 v180, v67
	v_mov_b32_e32 v181, v67
	v_mov_b32_e32 v182, 0
	v_mov_b32_e32 v183, v67
	v_mov_b32_e32 v184, v67
	v_mov_b32_e32 v185, v67
	v_mov_b32_e32 v186, 0
	v_mov_b32_e32 v187, v67
	v_mov_b32_e32 v188, v67
	v_mov_b32_e32 v189, v67
	v_mov_b32_e32 v190, 0
	v_mov_b32_e32 v191, v67
	v_mov_b32_e32 v192, v67
	v_mov_b32_e32 v193, v67
	s_barrier
	s_load_dwordx2 s[100:101], s[0:1], 0xc0
	v_readfirstlane_b32 s98, v0
	s_lshr_b32 s98, s98, 6
	s_lshl_b32 s99, s2, 3
	s_add_i32 s98, s98, s99
	v_and_b32_e32 v240, 63, v0
	v_lshrrev_b32_e32 v241, 4, v240
	v_and_b32_e32 v240, 15, v240
	v_lshlrev_b32_e32 v242, 4, v240
	v_lshl_add_u32 v242, v241, 12, v242
	v_lshl_add_u32 v243, v240, 2, v241
	v_lshlrev_b32_e32 v243, 10, v243
	s_lshl_b32 s99, s98, 16
	v_add_u32_e32 v250, s99, v242
	v_mov_b32_e32 v251, 0
	s_waitcnt lgkmcnt(0)
	v_lshl_add_u64 v[250:251], v[250:251], 0, s[100:101]
	s_load_dwordx2 s[100:101], s[0:1], 0xd8
	s_lshr_b32 s99, s98, 6
	s_lshl_b32 s99, s99, 20
	s_and_b32 s98, s98, 63
	s_lshl_b32 s98, s98, 4
	s_add_i32 s99, s99, s98
	s_add_i32 s99, s99, 0x11800000
	v_add_u32_e32 v252, s99, v243
	v_mov_b32_e32 v253, 0
	s_waitcnt lgkmcnt(0)
	v_lshl_add_u64 v[252:253], v[252:253], 0, s[100:101]
	s_mov_b32 s98, 16
	s_cmpk_eq_u32 s22, 0x100
	s_cselect_b32 s98, 0, s98
	s_branch .LBB0_687

.LBB0_716:
	s_ashr_i32 s39, s38, 31
	s_lshl_b64 s[66:67], s[38:39], 13
	v_lshl_or_b32 v20, s28, 7, v199
	s_add_u32 s66, s20, s66
	s_addc_u32 s67, s21, s67
	v_ashrrev_i32_e32 v21, 31, v20
	v_lshl_add_u64 v[6:7], v[20:21], 2, s[66:67]
	global_load_dwordx4 v[14:17], v[6:7], off
	global_load_dwordx4 v[10:13], v[6:7], off offset:16
	v_add_co_u32_e32 v2, vcc, s84, v6
	v_mov_b32_e32 v25, 0
	s_nop 0
	v_addc_co_u32_e32 v3, vcc, 0, v7, vcc
	v_lshl_add_u64 v[6:7], v[6:7], 0, s[50:51]
	global_load_dwordx4 v[2:5], v[2:3], off
	v_mov_b32_e32 v24, 0
	global_load_dwordx4 v[6:9], v[6:7], off offset:16
	v_lshl_add_u32 v22, v210, 8, v198
	v_ashrrev_i32_e32 v23, 31, v22
	v_lshlrev_b64 v[18:19], 10, v[22:23]
	v_lshl_add_u64 v[18:19], s[46:47], 0, v[18:19]
	v_lshl_add_u64 v[18:19], v[18:19], 0, v[20:21]
	v_or_b32_e32 v26, 16, v22
	v_ashrrev_i32_e32 v27, 31, v26
	s_waitcnt vmcnt(3)
	v_pk_fma_f32 v[30:31], v[190:191], s[54:55], v[14:15] op_sel_hi:[1,0,1]
	s_waitcnt vmcnt(2)
	v_pk_fma_f32 v[34:35], v[186:187], s[54:55], v[10:11] op_sel_hi:[1,0,1]
	v_pk_fma_f32 v[32:33], v[188:189], s[54:55], v[12:13] op_sel_hi:[1,0,1]
	v_min_f32_e32 v34, 0x40e00000, v34
	v_min_f32_e32 v35, 0x40e00000, v35
	v_pk_mul_f32 v[56:57], v[34:35], s[56:57] op_sel_hi:[1,0]
	v_min_f32_e32 v30, 0x40e00000, v30
	v_exp_f32_e32 v56, v56
	v_exp_f32_e32 v57, v57
	v_min_f32_e32 v31, 0x40e00000, v31
	v_min_f32_e32 v32, 0x40e00000, v32
	v_min_f32_e32 v33, 0x40e00000, v33
	v_pk_mul_f32 v[52:53], v[30:31], s[56:57] op_sel_hi:[1,0]
	v_pk_mul_f32 v[58:59], v[32:33], s[56:57] op_sel_hi:[1,0]
	v_exp_f32_e32 v52, v52
	v_exp_f32_e32 v53, v53
	v_exp_f32_e32 v58, v58
	v_exp_f32_e32 v59, v59
	v_pk_add_f32 v[56:57], v[56:57], 1.0 op_sel_hi:[1,0]
	v_pk_fma_f32 v[28:29], v[192:193], s[54:55], v[16:17] op_sel_hi:[1,0,1]
	v_rcp_f32_e32 v56, v56
	v_rcp_f32_e32 v57, v57
	v_min_f32_e32 v28, 0x40e00000, v28
	v_min_f32_e32 v29, 0x40e00000, v29
	s_waitcnt vmcnt(0)
	s_cmp_lt_u32 s98, 16
	s_cbranch_scc0 .Lgc_i9
	s_lshl_b32 s100, s98, 8
	s_mov_b32 s101, 0
	v_lshl_add_u64 v[240:241], v[250:251], 0, s[100:101]
	global_load_dwordx4 v[224:227], v[240:241], off
	s_add_u32 s100, s100, 0x4000
	v_lshl_add_u64 v[244:245], v[250:251], 0, s[100:101]
	global_load_dwordx4 v[228:231], v[244:245], off
	s_add_u32 s100, s100, 0x4000
	v_lshl_add_u64 v[246:247], v[250:251], 0, s[100:101]
	global_load_dwordx4 v[232:235], v[246:247], off
	s_add_u32 s100, s100, 0x4000
	v_lshl_add_u64 v[248:249], v[250:251], 0, s[100:101]
	global_load_dwordx4 v[236:239], v[248:249], off
.Lgc_i9:
	v_pk_fma_f32 v[50:51], v[154:155], s[54:55], v[6:7] op_sel_hi:[1,0,1]
	v_pk_mul_f32 v[54:55], v[28:29], s[56:57] op_sel_hi:[1,0]
	v_pk_add_f32 v[52:53], v[52:53], 1.0 op_sel_hi:[1,0]
	v_exp_f32_e32 v54, v54
	v_exp_f32_e32 v55, v55
	v_med3_f32 v50, v50, s85, v203
	v_med3_f32 v51, v51, s85, v203
	v_pk_add_f32 v[58:59], v[58:59], 1.0 op_sel_hi:[1,0]
	v_rcp_f32_e32 v52, v52
	v_rcp_f32_e32 v53, v53
	v_pk_add_f32 v[50:51], v[50:51], 1.0 op_sel_hi:[1,0]
	v_rcp_f32_e32 v58, v58
	v_rcp_f32_e32 v59, v59
	v_pk_mul_f32 v[34:35], v[34:35], v[56:57]
	v_pk_fma_f32 v[46:47], v[158:159], s[54:55], v[2:3] op_sel_hi:[1,0,1]
	v_pk_mul_f32 v[34:35], v[50:51], v[34:35]
	v_pk_fma_f32 v[48:49], v[156:157], s[54:55], v[8:9] op_sel_hi:[1,0,1]
	v_med3_f32 v46, v46, s85, v203
	v_med3_f32 v47, v47, s85, v203
	v_cvt_pk_fp8_f32 v25, v34, v35
	v_pk_fma_f32 v[38:39], v[182:183], s[54:55], v[14:15] op_sel_hi:[1,0,1]
	v_med3_f32 v48, v48, s85, v203
	v_med3_f32 v49, v49, s85, v203
	v_pk_add_f32 v[46:47], v[46:47], 1.0 op_sel_hi:[1,0]
	v_pk_add_f32 v[54:55], v[54:55], 1.0 op_sel_hi:[1,0]
	v_pk_mul_f32 v[30:31], v[30:31], v[52:53]
	v_min_f32_e32 v38, 0x40e00000, v38
	v_min_f32_e32 v39, 0x40e00000, v39
	v_pk_add_f32 v[48:49], v[48:49], 1.0 op_sel_hi:[1,0]
	v_rcp_f32_e32 v54, v54
	v_rcp_f32_e32 v55, v55
	v_pk_mul_f32 v[32:33], v[32:33], v[58:59]
	v_pk_mul_f32 v[30:31], v[46:47], v[30:31]
	v_pk_fma_f32 v[36:37], v[184:185], s[54:55], v[16:17] op_sel_hi:[1,0,1]
	v_pk_mul_f32 v[218:219], v[38:39], s[56:57] op_sel_hi:[1,0]
	v_cvt_pk_fp8_f32 v24, v30, v31
	v_pk_mul_f32 v[30:31], v[48:49], v[32:33]
	v_pk_fma_f32 v[44:45], v[160:161], s[54:55], v[4:5] op_sel_hi:[1,0,1]
	v_exp_f32_e32 v218, v218
	v_exp_f32_e32 v219, v219
	v_cvt_pk_fp8_f32 v25, v30, v31 op_sel:[0,0,1]
	v_min_f32_e32 v30, 0x40e00000, v36
	v_min_f32_e32 v31, 0x40e00000, v37
	v_med3_f32 v44, v44, s85, v203
	v_med3_f32 v45, v45, s85, v203
	v_pk_mul_f32 v[32:33], v[30:31], s[56:57] op_sel_hi:[1,0]
	v_pk_add_f32 v[44:45], v[44:45], 1.0 op_sel_hi:[1,0]
	v_pk_mul_f32 v[28:29], v[28:29], v[54:55]
	v_exp_f32_e32 v32, v32
	v_exp_f32_e32 v33, v33
	v_pk_mul_f32 v[28:29], v[44:45], v[28:29]
	v_pk_fma_f32 v[42:43], v[178:179], s[54:55], v[10:11] op_sel_hi:[1,0,1]
	v_cvt_pk_fp8_f32 v24, v28, v29 op_sel:[0,0,1]
	v_pk_add_f32 v[28:29], v[218:219], 1.0 op_sel_hi:[1,0]
	v_pk_add_f32 v[32:33], v[32:33], 1.0 op_sel_hi:[1,0]
	v_rcp_f32_e32 v28, v28
	v_rcp_f32_e32 v29, v29
	v_min_f32_e32 v34, 0x40e00000, v42
	v_min_f32_e32 v35, 0x40e00000, v43
	v_pk_fma_f32 v[62:63], v[150:151], s[54:55], v[2:3] op_sel_hi:[1,0,1]
	v_rcp_f32_e32 v32, v32
	v_rcp_f32_e32 v33, v33
	v_pk_mul_f32 v[36:37], v[34:35], s[56:57] op_sel_hi:[1,0]
	v_med3_f32 v62, v62, s85, v203
	v_med3_f32 v63, v63, s85, v203
	v_exp_f32_e32 v36, v36
	v_exp_f32_e32 v37, v37
	v_pk_fma_f32 v[60:61], v[152:153], s[54:55], v[4:5] op_sel_hi:[1,0,1]
	global_store_dwordx2 v[18:19], v[24:25], off
	v_pk_add_f32 v[24:25], v[62:63], 1.0 op_sel_hi:[1,0]
	v_pk_mul_f32 v[28:29], v[38:39], v[28:29]
	v_pk_mul_f32 v[30:31], v[30:31], v[32:33]
	v_pk_mul_f32 v[24:25], v[24:25], v[28:29]
	v_med3_f32 v28, v60, s85, v203
	v_med3_f32 v29, v61, s85, v203
	v_pk_add_f32 v[28:29], v[28:29], 1.0 op_sel_hi:[1,0]
	v_pk_fma_f32 v[40:41], v[180:181], s[54:55], v[12:13] op_sel_hi:[1,0,1]
	v_pk_mul_f32 v[28:29], v[28:29], v[30:31]
	v_pk_add_f32 v[30:31], v[36:37], 1.0 op_sel_hi:[1,0]
	v_mov_b32_e32 v38, 0
	v_rcp_f32_e32 v30, v30
	v_rcp_f32_e32 v31, v31
	v_cvt_pk_fp8_f32 v38, v24, v25
	v_pk_fma_f32 v[216:217], v[146:147], s[54:55], v[6:7] op_sel_hi:[1,0,1]
	v_mov_b32_e32 v39, 0
	v_pk_mul_f32 v[30:31], v[34:35], v[30:31]
	v_min_f32_e32 v34, 0x40e00000, v40
	v_min_f32_e32 v35, 0x40e00000, v41
	v_pk_mul_f32 v[36:37], v[34:35], s[56:57] op_sel_hi:[1,0]
	v_cvt_pk_fp8_f32 v38, v28, v29 op_sel:[0,0,1]
	v_exp_f32_e32 v36, v36
	v_exp_f32_e32 v37, v37
	v_pk_fma_f32 v[28:29], v[174:175], s[54:55], v[14:15] op_sel_hi:[1,0,1]
	v_med3_f32 v32, v216, s85, v203
	v_min_f32_e32 v28, 0x40e00000, v28
	v_pk_add_f32 v[36:37], v[36:37], 1.0 op_sel_hi:[1,0]
	v_min_f32_e32 v29, 0x40e00000, v29
	v_rcp_f32_e32 v36, v36
	v_rcp_f32_e32 v37, v37
	v_med3_f32 v33, v217, s85, v203
	v_pk_add_f32 v[32:33], v[32:33], 1.0 op_sel_hi:[1,0]
	v_pk_fma_f32 v[64:65], v[148:149], s[54:55], v[8:9] op_sel_hi:[1,0,1]
	v_pk_mul_f32 v[24:25], v[34:35], v[36:37]
	v_pk_mul_f32 v[36:37], v[28:29], s[56:57] op_sel_hi:[1,0]
	v_pk_mul_f32 v[30:31], v[32:33], v[30:31]
	v_exp_f32_e32 v36, v36
	v_exp_f32_e32 v37, v37
	v_cvt_pk_fp8_f32 v39, v30, v31
	v_med3_f32 v32, v64, s85, v203
	v_med3_f32 v33, v65, s85, v203
	v_pk_add_f32 v[36:37], v[36:37], 1.0 op_sel_hi:[1,0]
	v_pk_add_f32 v[32:33], v[32:33], 1.0 op_sel_hi:[1,0]
	v_rcp_f32_e32 v36, v36
	v_rcp_f32_e32 v37, v37
	v_pk_mul_f32 v[24:25], v[32:33], v[24:25]
	v_pk_fma_f32 v[32:33], v[170:171], s[54:55], v[10:11] op_sel_hi:[1,0,1]
	v_cvt_pk_fp8_f32 v39, v24, v25 op_sel:[0,0,1]
	v_lshlrev_b64 v[24:25], 10, v[26:27]
	v_pk_fma_f32 v[26:27], v[176:177], s[54:55], v[16:17] op_sel_hi:[1,0,1]
	v_pk_mul_f32 v[28:29], v[28:29], v[36:37]
	v_min_f32_e32 v26, 0x40e00000, v26
	v_min_f32_e32 v27, 0x40e00000, v27
	v_pk_mul_f32 v[36:37], v[26:27], s[56:57] op_sel_hi:[1,0]
	v_lshl_add_u64 v[24:25], s[46:47], 0, v[24:25]
	v_exp_f32_e32 v36, v36
	v_exp_f32_e32 v37, v37
	v_lshl_add_u64 v[24:25], v[24:25], 0, v[20:21]
	global_store_dwordx2 v[24:25], v[38:39], off
	v_pk_fma_f32 v[38:39], v[142:143], s[54:55], v[2:3] op_sel_hi:[1,0,1]
	v_pk_add_f32 v[36:37], v[36:37], 1.0 op_sel_hi:[1,0]
	v_med3_f32 v38, v38, s85, v203
	v_med3_f32 v39, v39, s85, v203
	v_pk_add_f32 v[38:39], v[38:39], 1.0 op_sel_hi:[1,0]
	v_min_f32_e32 v32, 0x40e00000, v32
	v_min_f32_e32 v33, 0x40e00000, v33
	v_pk_mul_f32 v[28:29], v[38:39], v[28:29]
	v_rcp_f32_e32 v36, v36
	v_rcp_f32_e32 v37, v37
	v_pk_mul_f32 v[38:39], v[32:33], s[56:57] op_sel_hi:[1,0]
	v_pk_fma_f32 v[34:35], v[144:145], s[54:55], v[4:5] op_sel_hi:[1,0,1]
	v_exp_f32_e32 v38, v38
	v_exp_f32_e32 v39, v39
	v_med3_f32 v34, v34, s85, v203
	v_med3_f32 v35, v35, s85, v203
	v_pk_add_f32 v[34:35], v[34:35], 1.0 op_sel_hi:[1,0]
	v_pk_mul_f32 v[26:27], v[26:27], v[36:37]
	v_pk_fma_f32 v[30:31], v[172:173], s[54:55], v[12:13] op_sel_hi:[1,0,1]
	v_pk_mul_f32 v[26:27], v[34:35], v[26:27]
	v_pk_add_f32 v[34:35], v[38:39], 1.0 op_sel_hi:[1,0]
	v_min_f32_e32 v30, 0x40e00000, v30
	v_rcp_f32_e32 v34, v34
	v_rcp_f32_e32 v35, v35
	v_min_f32_e32 v31, 0x40e00000, v31
	v_mov_b32_e32 v38, 0
	v_cvt_pk_fp8_f32 v38, v28, v29
	v_pk_mul_f32 v[32:33], v[32:33], v[34:35]
	v_pk_mul_f32 v[34:35], v[30:31], s[56:57] op_sel_hi:[1,0]
	v_pk_fma_f32 v[42:43], v[138:139], s[54:55], v[6:7] op_sel_hi:[1,0,1]
	v_exp_f32_e32 v34, v34
	v_exp_f32_e32 v35, v35
	v_med3_f32 v36, v42, s85, v203
	v_med3_f32 v37, v43, s85, v203
	v_pk_add_f32 v[36:37], v[36:37], 1.0 op_sel_hi:[1,0]
	v_pk_add_f32 v[34:35], v[34:35], 1.0 op_sel_hi:[1,0]
	v_cvt_pk_fp8_f32 v38, v26, v27 op_sel:[0,0,1]
	v_rcp_f32_e32 v34, v34
	v_rcp_f32_e32 v35, v35
	v_pk_fma_f32 v[26:27], v[166:167], s[54:55], v[14:15] op_sel_hi:[1,0,1]
	v_pk_mul_f32 v[32:33], v[36:37], v[32:33]
	v_mov_b32_e32 v39, 0
	v_min_f32_e32 v26, 0x40e00000, v26
	v_min_f32_e32 v27, 0x40e00000, v27
	v_pk_fma_f32 v[40:41], v[140:141], s[54:55], v[8:9] op_sel_hi:[1,0,1]
	v_cvt_pk_fp8_f32 v39, v32, v33
	v_pk_mul_f32 v[28:29], v[30:31], v[34:35]
	v_pk_mul_f32 v[34:35], v[26:27], s[56:57] op_sel_hi:[1,0]
	v_med3_f32 v36, v40, s85, v203
	v_med3_f32 v37, v41, s85, v203
	v_exp_f32_e32 v34, v34
	v_exp_f32_e32 v35, v35
	v_pk_add_f32 v[36:37], v[36:37], 1.0 op_sel_hi:[1,0]
	v_or_b32_e32 v24, 32, v22
	v_pk_mul_f32 v[28:29], v[36:37], v[28:29]
	v_ashrrev_i32_e32 v25, 31, v24
	v_cvt_pk_fp8_f32 v39, v28, v29 op_sel:[0,0,1]
	v_lshlrev_b64 v[24:25], 10, v[24:25]
	v_pk_add_f32 v[34:35], v[34:35], 1.0 op_sel_hi:[1,0]
	v_lshl_add_u64 v[24:25], s[46:47], 0, v[24:25]
	v_rcp_f32_e32 v34, v34
	v_rcp_f32_e32 v35, v35
	v_lshl_add_u64 v[24:25], v[24:25], 0, v[20:21]
	global_store_dwordx2 v[24:25], v[38:39], off
	v_pk_fma_f32 v[24:25], v[168:169], s[54:55], v[16:17] op_sel_hi:[1,0,1]
	v_pk_mul_f32 v[26:27], v[26:27], v[34:35]
	v_min_f32_e32 v24, 0x40e00000, v24
	v_min_f32_e32 v25, 0x40e00000, v25
	v_pk_mul_f32 v[34:35], v[24:25], s[56:57] op_sel_hi:[1,0]
	v_pk_fma_f32 v[36:37], v[134:135], s[54:55], v[2:3] op_sel_hi:[1,0,1]
	v_exp_f32_e32 v34, v34
	v_exp_f32_e32 v35, v35
	v_pk_fma_f32 v[30:31], v[162:163], s[54:55], v[10:11] op_sel_hi:[1,0,1]
	v_med3_f32 v36, v36, s85, v203
	v_med3_f32 v37, v37, s85, v203
	v_pk_add_f32 v[36:37], v[36:37], 1.0 op_sel_hi:[1,0]
	v_pk_add_f32 v[34:35], v[34:35], 1.0 op_sel_hi:[1,0]
	v_min_f32_e32 v30, 0x40e00000, v30
	v_min_f32_e32 v31, 0x40e00000, v31
	v_pk_mul_f32 v[26:27], v[36:37], v[26:27]
	v_rcp_f32_e32 v34, v34
	v_rcp_f32_e32 v35, v35
	v_pk_mul_f32 v[36:37], v[30:31], s[56:57] op_sel_hi:[1,0]
	v_pk_fma_f32 v[32:33], v[136:137], s[54:55], v[4:5] op_sel_hi:[1,0,1]
	v_exp_f32_e32 v36, v36
	v_exp_f32_e32 v37, v37
	v_med3_f32 v32, v32, s85, v203
	v_med3_f32 v33, v33, s85, v203
	v_pk_add_f32 v[32:33], v[32:33], 1.0 op_sel_hi:[1,0]
	v_pk_mul_f32 v[24:25], v[24:25], v[34:35]
	v_pk_fma_f32 v[28:29], v[164:165], s[54:55], v[12:13] op_sel_hi:[1,0,1]
	v_pk_mul_f32 v[24:25], v[32:33], v[24:25]
	v_pk_add_f32 v[32:33], v[36:37], 1.0 op_sel_hi:[1,0]
	v_min_f32_e32 v28, 0x40e00000, v28
	v_rcp_f32_e32 v32, v32
	v_rcp_f32_e32 v33, v33
	v_min_f32_e32 v29, 0x40e00000, v29
	v_or_b32_e32 v22, 48, v22
	v_ashrrev_i32_e32 v23, 31, v22
	v_pk_mul_f32 v[30:31], v[30:31], v[32:33]
	v_pk_mul_f32 v[32:33], v[28:29], s[56:57] op_sel_hi:[1,0]
	v_pk_fma_f32 v[40:41], v[130:131], s[54:55], v[6:7] op_sel_hi:[1,0,1]
	v_exp_f32_e32 v32, v32
	v_exp_f32_e32 v33, v33
	v_lshlrev_b64 v[22:23], 10, v[22:23]
	v_med3_f32 v34, v40, s85, v203
	v_med3_f32 v35, v41, s85, v203
	v_pk_add_f32 v[32:33], v[32:33], 1.0 op_sel_hi:[1,0]
	v_lshl_add_u64 v[22:23], s[46:47], 0, v[22:23]
	v_pk_add_f32 v[34:35], v[34:35], 1.0 op_sel_hi:[1,0]
	v_rcp_f32_e32 v32, v32
	v_rcp_f32_e32 v33, v33
	v_lshl_add_u64 v[20:21], v[22:23], 0, v[20:21]
	v_pk_fma_f32 v[22:23], v[126:127], s[54:55], v[14:15] op_sel_hi:[1,0,1]
	v_pk_mul_f32 v[30:31], v[34:35], v[30:31]
	v_mov_b32_e32 v36, 0
	v_mov_b32_e32 v37, 0
	v_min_f32_e32 v22, 0x40e00000, v22
	v_min_f32_e32 v23, 0x40e00000, v23
	v_pk_fma_f32 v[38:39], v[132:133], s[54:55], v[8:9] op_sel_hi:[1,0,1]
	v_cvt_pk_fp8_f32 v36, v26, v27
	v_cvt_pk_fp8_f32 v37, v30, v31
	v_pk_mul_f32 v[30:31], v[22:23], s[56:57] op_sel_hi:[1,0]
	v_med3_f32 v34, v38, s85, v203
	v_med3_f32 v35, v39, s85, v203
	v_exp_f32_e32 v30, v30
	v_exp_f32_e32 v31, v31
	v_pk_add_f32 v[34:35], v[34:35], 1.0 op_sel_hi:[1,0]
	v_pk_mul_f32 v[26:27], v[28:29], v[32:33]
	v_cvt_pk_fp8_f32 v36, v24, v25 op_sel:[0,0,1]
	v_pk_mul_f32 v[26:27], v[34:35], v[26:27]
	v_pk_add_f32 v[30:31], v[30:31], 1.0 op_sel_hi:[1,0]
	v_cvt_pk_fp8_f32 v37, v26, v27 op_sel:[0,0,1]
	v_rcp_f32_e32 v30, v30
	v_rcp_f32_e32 v31, v31
	v_pk_fma_f32 v[32:33], v[94:95], s[54:55], v[2:3] op_sel_hi:[1,0,1]
	global_store_dwordx2 v[20:21], v[36:37], off
	v_pk_fma_f32 v[20:21], v[128:129], s[54:55], v[16:17] op_sel_hi:[1,0,1]
	v_pk_mul_f32 v[22:23], v[22:23], v[30:31]
	v_min_f32_e32 v20, 0x40e00000, v20
	v_min_f32_e32 v21, 0x40e00000, v21
	v_pk_mul_f32 v[30:31], v[20:21], s[56:57] op_sel_hi:[1,0]
	v_pk_fma_f32 v[26:27], v[122:123], s[54:55], v[10:11] op_sel_hi:[1,0,1]
	v_exp_f32_e32 v30, v30
	v_exp_f32_e32 v31, v31
	v_med3_f32 v32, v32, s85, v203
	v_med3_f32 v33, v33, s85, v203
	v_pk_add_f32 v[32:33], v[32:33], 1.0 op_sel_hi:[1,0]
	v_pk_add_f32 v[30:31], v[30:31], 1.0 op_sel_hi:[1,0]
	v_min_f32_e32 v26, 0x40e00000, v26
	v_min_f32_e32 v27, 0x40e00000, v27
	v_pk_mul_f32 v[22:23], v[32:33], v[22:23]
	v_rcp_f32_e32 v30, v30
	v_rcp_f32_e32 v31, v31
	v_pk_mul_f32 v[32:33], v[26:27], s[56:57] op_sel_hi:[1,0]
	v_pk_fma_f32 v[28:29], v[96:97], s[54:55], v[4:5] op_sel_hi:[1,0,1]
	v_exp_f32_e32 v32, v32
	v_exp_f32_e32 v33, v33
	v_med3_f32 v28, v28, s85, v203
	v_med3_f32 v29, v29, s85, v203
	v_pk_add_f32 v[28:29], v[28:29], 1.0 op_sel_hi:[1,0]
	v_pk_mul_f32 v[20:21], v[20:21], v[30:31]
	v_pk_fma_f32 v[24:25], v[124:125], s[54:55], v[12:13] op_sel_hi:[1,0,1]
	v_pk_mul_f32 v[20:21], v[28:29], v[20:21]
	v_pk_add_f32 v[28:29], v[32:33], 1.0 op_sel_hi:[1,0]
	v_min_f32_e32 v24, 0x40e00000, v24
	v_rcp_f32_e32 v28, v28
	v_rcp_f32_e32 v29, v29
	v_min_f32_e32 v25, 0x40e00000, v25
	v_pk_fma_f32 v[36:37], v[90:91], s[54:55], v[6:7] op_sel_hi:[1,0,1]
	v_mov_b32_e32 v33, 0
	v_pk_mul_f32 v[26:27], v[26:27], v[28:29]
	v_pk_mul_f32 v[28:29], v[24:25], s[56:57] op_sel_hi:[1,0]
	v_med3_f32 v30, v36, s85, v203
	v_exp_f32_e32 v28, v28
	v_exp_f32_e32 v29, v29
	v_med3_f32 v31, v37, s85, v203
	v_pk_add_f32 v[30:31], v[30:31], 1.0 op_sel_hi:[1,0]
	v_pk_fma_f32 v[34:35], v[92:93], s[54:55], v[8:9] op_sel_hi:[1,0,1]
	v_pk_add_f32 v[28:29], v[28:29], 1.0 op_sel_hi:[1,0]
	v_pk_mul_f32 v[26:27], v[30:31], v[26:27]
	v_rcp_f32_e32 v28, v28
	v_rcp_f32_e32 v29, v29
	v_cvt_pk_fp8_f32 v33, v26, v27
	v_med3_f32 v30, v34, s85, v203
	v_med3_f32 v31, v35, s85, v203
	v_mov_b32_e32 v32, 0
	v_pk_add_f32 v[30:31], v[30:31], 1.0 op_sel_hi:[1,0]
	v_cvt_pk_fp8_f32 v32, v22, v23
	v_pk_mul_f32 v[22:23], v[24:25], v[28:29]
	v_pk_fma_f32 v[26:27], v[114:115], s[54:55], v[10:11] op_sel_hi:[1,0,1]
	v_pk_mul_f32 v[22:23], v[30:31], v[22:23]
	v_cvt_pk_fp8_f32 v32, v20, v21 op_sel:[0,0,1]
	v_cvt_pk_fp8_f32 v33, v22, v23 op_sel:[0,0,1]
	v_pk_fma_f32 v[22:23], v[118:119], s[54:55], v[14:15] op_sel_hi:[1,0,1]
	v_add_co_u32_e32 v20, vcc, s83, v18
	v_min_f32_e32 v22, 0x40e00000, v22
	v_min_f32_e32 v23, 0x40e00000, v23
	v_pk_mul_f32 v[30:31], v[22:23], s[56:57] op_sel_hi:[1,0]
	v_addc_co_u32_e32 v21, vcc, 0, v19, vcc
	v_exp_f32_e32 v30, v30
	v_exp_f32_e32 v31, v31
	global_store_dwordx2 v[20:21], v[32:33], off
	v_pk_fma_f32 v[20:21], v[120:121], s[54:55], v[16:17] op_sel_hi:[1,0,1]
	v_pk_fma_f32 v[32:33], v[86:87], s[54:55], v[2:3] op_sel_hi:[1,0,1]
	v_pk_add_f32 v[30:31], v[30:31], 1.0 op_sel_hi:[1,0]
	v_min_f32_e32 v20, 0x40e00000, v20
	v_rcp_f32_e32 v30, v30
	v_rcp_f32_e32 v31, v31
	v_min_f32_e32 v21, 0x40e00000, v21
	v_med3_f32 v32, v32, s85, v203
	v_med3_f32 v33, v33, s85, v203
	v_pk_mul_f32 v[22:23], v[22:23], v[30:31]
	v_pk_mul_f32 v[30:31], v[20:21], s[56:57] op_sel_hi:[1,0]
	v_pk_add_f32 v[32:33], v[32:33], 1.0 op_sel_hi:[1,0]
	v_exp_f32_e32 v30, v30
	v_exp_f32_e32 v31, v31
	v_min_f32_e32 v26, 0x40e00000, v26
	v_min_f32_e32 v27, 0x40e00000, v27
	v_pk_mul_f32 v[22:23], v[32:33], v[22:23]
	v_pk_add_f32 v[30:31], v[30:31], 1.0 op_sel_hi:[1,0]
	v_pk_mul_f32 v[32:33], v[26:27], s[56:57] op_sel_hi:[1,0]
	v_rcp_f32_e32 v30, v30
	v_rcp_f32_e32 v31, v31
	v_exp_f32_e32 v32, v32
	v_exp_f32_e32 v33, v33
	v_pk_fma_f32 v[28:29], v[88:89], s[54:55], v[4:5] op_sel_hi:[1,0,1]
	v_pk_mul_f32 v[20:21], v[20:21], v[30:31]
	v_med3_f32 v28, v28, s85, v203
	v_med3_f32 v29, v29, s85, v203
	v_pk_add_f32 v[28:29], v[28:29], 1.0 op_sel_hi:[1,0]
	v_pk_fma_f32 v[24:25], v[116:117], s[54:55], v[12:13] op_sel_hi:[1,0,1]
	v_pk_mul_f32 v[20:21], v[28:29], v[20:21]
	v_pk_add_f32 v[28:29], v[32:33], 1.0 op_sel_hi:[1,0]
	v_min_f32_e32 v24, 0x40e00000, v24
	v_rcp_f32_e32 v28, v28
	v_rcp_f32_e32 v29, v29
	v_min_f32_e32 v25, 0x40e00000, v25
	v_pk_fma_f32 v[36:37], v[82:83], s[54:55], v[6:7] op_sel_hi:[1,0,1]
	v_mov_b32_e32 v33, 0
	v_pk_mul_f32 v[26:27], v[26:27], v[28:29]
	v_pk_mul_f32 v[28:29], v[24:25], s[56:57] op_sel_hi:[1,0]
	v_med3_f32 v30, v36, s85, v203
	v_exp_f32_e32 v28, v28
	v_exp_f32_e32 v29, v29
	v_med3_f32 v31, v37, s85, v203
	v_pk_add_f32 v[30:31], v[30:31], 1.0 op_sel_hi:[1,0]
	v_pk_fma_f32 v[34:35], v[84:85], s[54:55], v[8:9] op_sel_hi:[1,0,1]
	v_pk_add_f32 v[28:29], v[28:29], 1.0 op_sel_hi:[1,0]
	v_pk_mul_f32 v[26:27], v[30:31], v[26:27]
	v_rcp_f32_e32 v28, v28
	v_rcp_f32_e32 v29, v29
	v_cvt_pk_fp8_f32 v33, v26, v27
	v_med3_f32 v30, v34, s85, v203
	v_med3_f32 v31, v35, s85, v203
	v_mov_b32_e32 v32, 0
	v_pk_add_f32 v[30:31], v[30:31], 1.0 op_sel_hi:[1,0]
	v_cvt_pk_fp8_f32 v32, v22, v23
	v_pk_mul_f32 v[22:23], v[24:25], v[28:29]
	v_pk_fma_f32 v[26:27], v[106:107], s[54:55], v[10:11] op_sel_hi:[1,0,1]
	v_pk_mul_f32 v[22:23], v[30:31], v[22:23]
	v_cvt_pk_fp8_f32 v32, v20, v21 op_sel:[0,0,1]
	v_cvt_pk_fp8_f32 v33, v22, v23 op_sel:[0,0,1]
	v_pk_fma_f32 v[22:23], v[110:111], s[54:55], v[14:15] op_sel_hi:[1,0,1]
	v_add_co_u32_e32 v20, vcc, s86, v18
	v_min_f32_e32 v22, 0x40e00000, v22
	v_min_f32_e32 v23, 0x40e00000, v23
	v_pk_mul_f32 v[30:31], v[22:23], s[56:57] op_sel_hi:[1,0]
	v_addc_co_u32_e32 v21, vcc, 0, v19, vcc
	v_exp_f32_e32 v30, v30
	v_exp_f32_e32 v31, v31
	global_store_dwordx2 v[20:21], v[32:33], off
	v_pk_fma_f32 v[20:21], v[112:113], s[54:55], v[16:17] op_sel_hi:[1,0,1]
	v_pk_fma_f32 v[32:33], v[78:79], s[54:55], v[2:3] op_sel_hi:[1,0,1]
	v_pk_add_f32 v[30:31], v[30:31], 1.0 op_sel_hi:[1,0]
	v_min_f32_e32 v20, 0x40e00000, v20
	v_rcp_f32_e32 v30, v30
	v_rcp_f32_e32 v31, v31
	v_min_f32_e32 v21, 0x40e00000, v21
	v_med3_f32 v32, v32, s85, v203
	v_med3_f32 v33, v33, s85, v203
	v_pk_mul_f32 v[22:23], v[22:23], v[30:31]
	v_pk_mul_f32 v[30:31], v[20:21], s[56:57] op_sel_hi:[1,0]
	v_pk_add_f32 v[32:33], v[32:33], 1.0 op_sel_hi:[1,0]
	v_exp_f32_e32 v30, v30
	v_exp_f32_e32 v31, v31
	v_min_f32_e32 v26, 0x40e00000, v26
	v_min_f32_e32 v27, 0x40e00000, v27
	v_pk_mul_f32 v[22:23], v[32:33], v[22:23]
	v_pk_add_f32 v[30:31], v[30:31], 1.0 op_sel_hi:[1,0]
	v_pk_mul_f32 v[32:33], v[26:27], s[56:57] op_sel_hi:[1,0]
	v_rcp_f32_e32 v30, v30
	v_rcp_f32_e32 v31, v31
	v_exp_f32_e32 v32, v32
	v_exp_f32_e32 v33, v33
	v_pk_fma_f32 v[28:29], v[80:81], s[54:55], v[4:5] op_sel_hi:[1,0,1]
	v_pk_mul_f32 v[20:21], v[20:21], v[30:31]
	v_med3_f32 v28, v28, s85, v203
	v_med3_f32 v29, v29, s85, v203
	v_pk_add_f32 v[28:29], v[28:29], 1.0 op_sel_hi:[1,0]
	v_pk_fma_f32 v[24:25], v[108:109], s[54:55], v[12:13] op_sel_hi:[1,0,1]
	v_pk_mul_f32 v[20:21], v[28:29], v[20:21]
	v_pk_add_f32 v[28:29], v[32:33], 1.0 op_sel_hi:[1,0]
	v_min_f32_e32 v24, 0x40e00000, v24
	v_rcp_f32_e32 v28, v28
	v_rcp_f32_e32 v29, v29
	v_min_f32_e32 v25, 0x40e00000, v25
	v_pk_fma_f32 v[36:37], v[74:75], s[54:55], v[6:7] op_sel_hi:[1,0,1]
	v_mov_b32_e32 v32, 0
	v_pk_mul_f32 v[26:27], v[26:27], v[28:29]
	v_pk_mul_f32 v[28:29], v[24:25], s[56:57] op_sel_hi:[1,0]
	v_med3_f32 v30, v36, s85, v203
	v_exp_f32_e32 v28, v28
	v_exp_f32_e32 v29, v29
	v_med3_f32 v31, v37, s85, v203
	v_pk_add_f32 v[30:31], v[30:31], 1.0 op_sel_hi:[1,0]
	v_mov_b32_e32 v33, 0
	v_pk_add_f32 v[28:29], v[28:29], 1.0 op_sel_hi:[1,0]
	v_pk_mul_f32 v[26:27], v[30:31], v[26:27]
	v_rcp_f32_e32 v28, v28
	v_rcp_f32_e32 v29, v29
	v_pk_fma_f32 v[34:35], v[76:77], s[54:55], v[8:9] op_sel_hi:[1,0,1]
	v_cvt_pk_fp8_f32 v32, v22, v23
	v_cvt_pk_fp8_f32 v33, v26, v27
	v_med3_f32 v30, v34, s85, v203
	v_med3_f32 v31, v35, s85, v203
	v_pk_add_f32 v[30:31], v[30:31], 1.0 op_sel_hi:[1,0]
	v_pk_mul_f32 v[22:23], v[24:25], v[28:29]
	v_cvt_pk_fp8_f32 v32, v20, v21 op_sel:[0,0,1]
	v_pk_mul_f32 v[22:23], v[30:31], v[22:23]
	v_add_co_u32_e32 v20, vcc, s87, v18
	v_cvt_pk_fp8_f32 v33, v22, v23 op_sel:[0,0,1]
	v_pk_fma_f32 v[14:15], v[102:103], s[54:55], v[14:15] op_sel_hi:[1,0,1]
	v_addc_co_u32_e32 v21, vcc, 0, v19, vcc
	v_min_f32_e32 v14, 0x40e00000, v14
	v_min_f32_e32 v15, 0x40e00000, v15
	global_store_dwordx2 v[20:21], v[32:33], off
	v_pk_mul_f32 v[20:21], v[14:15], s[56:57] op_sel_hi:[1,0]
	v_pk_fma_f32 v[16:17], v[104:105], s[54:55], v[16:17] op_sel_hi:[1,0,1]
	v_exp_f32_e32 v20, v20
	v_exp_f32_e32 v21, v21
	v_min_f32_e32 v16, 0x40e00000, v16
	v_min_f32_e32 v17, 0x40e00000, v17
	v_pk_fma_f32 v[2:3], v[70:71], s[54:55], v[2:3] op_sel_hi:[1,0,1]
	v_pk_add_f32 v[20:21], v[20:21], 1.0 op_sel_hi:[1,0]
	v_med3_f32 v2, v2, s85, v203
	v_rcp_f32_e32 v20, v20
	v_rcp_f32_e32 v21, v21
	v_med3_f32 v3, v3, s85, v203
	v_pk_fma_f32 v[10:11], v[98:99], s[54:55], v[10:11] op_sel_hi:[1,0,1]
	v_pk_add_f32 v[2:3], v[2:3], 1.0 op_sel_hi:[1,0]
	v_pk_mul_f32 v[14:15], v[14:15], v[20:21]
	v_pk_mul_f32 v[20:21], v[16:17], s[56:57] op_sel_hi:[1,0]
	v_pk_mul_f32 v[2:3], v[2:3], v[14:15]
	v_exp_f32_e32 v20, v20
	v_exp_f32_e32 v21, v21
	v_min_f32_e32 v10, 0x40e00000, v10
	v_min_f32_e32 v11, 0x40e00000, v11
	v_pk_fma_f32 v[4:5], v[72:73], s[54:55], v[4:5] op_sel_hi:[1,0,1]
	v_pk_add_f32 v[14:15], v[20:21], 1.0 op_sel_hi:[1,0]
	v_pk_mul_f32 v[20:21], v[10:11], s[56:57] op_sel_hi:[1,0]
	v_rcp_f32_e32 v14, v14
	v_rcp_f32_e32 v15, v15
	v_exp_f32_e32 v20, v20
	v_exp_f32_e32 v21, v21
	v_med3_f32 v4, v4, s85, v203
	v_med3_f32 v5, v5, s85, v203
	v_pk_add_f32 v[4:5], v[4:5], 1.0 op_sel_hi:[1,0]
	v_pk_mul_f32 v[14:15], v[16:17], v[14:15]
	v_pk_fma_f32 v[12:13], v[100:101], s[54:55], v[12:13] op_sel_hi:[1,0,1]
	v_pk_mul_f32 v[4:5], v[4:5], v[14:15]
	v_pk_add_f32 v[14:15], v[20:21], 1.0 op_sel_hi:[1,0]
	v_min_f32_e32 v12, 0x40e00000, v12
	v_rcp_f32_e32 v14, v14
	v_rcp_f32_e32 v15, v15
	v_min_f32_e32 v13, 0x40e00000, v13
	v_pk_fma_f32 v[6:7], v[66:67], s[54:55], v[6:7] op_sel_hi:[1,0,1]
	v_pk_fma_f32 v[8:9], v[68:69], s[54:55], v[8:9] op_sel_hi:[1,0,1]
	v_pk_mul_f32 v[10:11], v[10:11], v[14:15]
	v_pk_mul_f32 v[14:15], v[12:13], s[56:57] op_sel_hi:[1,0]
	v_med3_f32 v6, v6, s85, v203
	v_exp_f32_e32 v14, v14
	v_exp_f32_e32 v15, v15
	v_med3_f32 v7, v7, s85, v203
	v_pk_add_f32 v[6:7], v[6:7], 1.0 op_sel_hi:[1,0]
	v_med3_f32 v8, v8, s85, v203
	v_pk_mul_f32 v[6:7], v[6:7], v[10:11]
	v_pk_add_f32 v[10:11], v[14:15], 1.0 op_sel_hi:[1,0]
	v_mov_b32_e32 v14, 0
	v_rcp_f32_e32 v10, v10
	v_rcp_f32_e32 v11, v11
	v_mov_b32_e32 v15, 0
	v_cvt_pk_fp8_f32 v14, v2, v3
	v_cvt_pk_fp8_f32 v15, v6, v7
	v_med3_f32 v9, v9, s85, v203
	v_pk_add_f32 v[8:9], v[8:9], 1.0 op_sel_hi:[1,0]
	v_pk_mul_f32 v[2:3], v[12:13], v[10:11]
	v_cvt_pk_fp8_f32 v14, v4, v5 op_sel:[0,0,1]
	v_pk_mul_f32 v[2:3], v[8:9], v[2:3]
	v_mov_b32_e32 v5, v214
	v_cvt_pk_fp8_f32 v15, v2, v3 op_sel:[0,0,1]
	v_add_co_u32_e32 v2, vcc, 0x2c000, v18
	v_mov_b32_e32 v4, v212
	s_nop 0
	v_addc_co_u32_e32 v3, vcc, 0, v19, vcc
	global_store_dwordx2 v[2:3], v[14:15], off
	s_and_b64 vcc, exec, s[4:5]
	v_mov_b32_e32 v2, v213
	v_mov_b32_e32 v3, v211
	s_cbranch_vccnz .LBB0_718
	v_mov_b32_e32 v2, v194
	s_nop 0
	v_ashrrev_i32_e32 v3, 31, v2
	v_lshrrev_b32_e32 v3, 26, v3
	v_lshlrev_b32_e32 v4, 4, v2
	v_add_u32_e32 v3, v2, v3
	v_bfe_i32 v2, v2, 27, 1
	v_lshrrev_b32_e32 v2, 22, v2
	v_add_u32_e32 v2, v4, v2
	v_and_b32_e32 v2, 0xfffffc00, v2
	v_sub_u32_e32 v2, v4, v2
	v_lshrrev_b32_e32 v5, 4, v2
	v_bitop3_b32 v5, v5, v2, 32 bitop3:0x6c
	v_ashrrev_i32_e32 v2, 31, v2
	v_lshrrev_b32_e32 v2, 26, v2
	v_add_u32_e32 v2, v5, v2
	v_and_b32_e32 v2, 0xc0, v2
	v_add_u32_e32 v4, 0x2000, v4
	v_sub_u32_e32 v2, v5, v2
	v_ashrrev_i32_e32 v5, 31, v4
	v_lshrrev_b32_e32 v5, 22, v5
	v_add_u32_e32 v5, v4, v5
	v_ashrrev_i32_e32 v5, 10, v5
	v_mul_i32_i24_e32 v6, 0x400, v5
	v_sub_u32_e32 v4, v4, v6
	v_lshrrev_b32_e32 v6, 4, v4
	v_bitop3_b32 v6, v6, v4, 32 bitop3:0x6c
	v_ashrrev_i32_e32 v4, 31, v4
	v_lshrrev_b32_e32 v4, 26, v4
	v_add_u32_e32 v4, v6, v4
	v_and_b32_e32 v4, 0xc0, v4
	v_sub_u32_e32 v4, v6, v4
	v_lshrrev_b32_e32 v3, 1, v3
	v_ashrrev_i16_sdwa v2, v195, sext(v2) dst_sel:DWORD dst_unused:UNUSED_PAD src0_sel:DWORD src1_sel:BYTE_0
	v_lshlrev_b32_e32 v5, 5, v5
	v_ashrrev_i16_sdwa v4, v195, sext(v4) dst_sel:DWORD dst_unused:UNUSED_PAD src0_sel:DWORD src1_sel:BYTE_0
	v_and_b32_e32 v3, 32, v3
	v_bfe_i32 v2, v2, 0, 16
	v_and_b32_e32 v5, 32, v5
	v_bfe_i32 v4, v4, 0, 16
	v_add_lshl_u32 v2, v3, v2, 1
	v_add_lshl_u32 v5, v5, v4, 1
	v_lshl_add_u32 v3, v205, 10, v2
	v_lshl_add_u32 v2, v204, 10, v2
	v_lshl_add_u32 v4, v209, 10, v5
	v_lshl_add_u32 v5, v207, 10, v5
.LBB0_718:
	s_waitcnt vmcnt(8)
	s_cmp_lt_u32 s98, 16
	s_cbranch_scc0 .Lgc_c9
	v_mul_f32_e32 v224, 0x42000000, v224
	v_mul_f32_e32 v225, 0x42000000, v225
	v_mul_f32_e32 v226, 0x42000000, v226
	v_mul_f32_e32 v227, 0x42000000, v227
	v_mul_f32_e32 v228, 0x42000000, v228
	v_mul_f32_e32 v229, 0x42000000, v229
	v_mul_f32_e32 v230, 0x42000000, v230
	v_mul_f32_e32 v231, 0x42000000, v231
	v_mul_f32_e32 v232, 0x42000000, v232
	v_mul_f32_e32 v233, 0x42000000, v233
	v_mul_f32_e32 v234, 0x42000000, v234
	v_mul_f32_e32 v235, 0x42000000, v235
	v_mul_f32_e32 v236, 0x42000000, v236
	v_mul_f32_e32 v237, 0x42000000, v237
	v_mul_f32_e32 v238, 0x42000000, v238
	v_mul_f32_e32 v239, 0x42000000, v239
	s_nop 1
	v_permlane32_swap_b32_e32 v224, v226
	v_permlane32_swap_b32_e32 v225, v227
	v_permlane32_swap_b32_e32 v228, v230
	v_permlane32_swap_b32_e32 v229, v231
	v_permlane32_swap_b32_e32 v232, v234
	v_permlane32_swap_b32_e32 v233, v235
	v_permlane32_swap_b32_e32 v236, v238
	v_permlane32_swap_b32_e32 v237, v239
	s_nop 1
	v_permlane16_swap_b32_e32 v224, v225
	v_permlane16_swap_b32_e32 v226, v227
	v_permlane16_swap_b32_e32 v228, v229
	v_permlane16_swap_b32_e32 v230, v231
	v_permlane16_swap_b32_e32 v232, v233
	v_permlane16_swap_b32_e32 v234, v235
	v_permlane16_swap_b32_e32 v236, v237
	v_permlane16_swap_b32_e32 v238, v239
	s_nop 1
	v_cvt_pk_fp8_f32 v244, v224, v225
	v_cvt_pk_fp8_f32 v244, v226, v227 op_sel:[0,0,1]
	v_cvt_pk_fp8_f32 v245, v228, v229
	v_cvt_pk_fp8_f32 v245, v230, v231 op_sel:[0,0,1]
	v_cvt_pk_fp8_f32 v246, v232, v233
	v_cvt_pk_fp8_f32 v246, v234, v235 op_sel:[0,0,1]
	v_cvt_pk_fp8_f32 v247, v236, v237
	v_cvt_pk_fp8_f32 v247, v238, v239 op_sel:[0,0,1]
	s_lshl_b32 s100, s98, 16
	s_mov_b32 s101, 0
	v_lshl_add_u64 v[240:241], v[252:253], 0, s[100:101]
	global_store_dwordx4 v[240:241], v[244:247], off
	s_add_i32 s98, s98, 1
.Lgc_c9:
	s_waitcnt lgkmcnt(0)
	s_andn2_b64 vcc, exec, s[42:43]
	s_cbranch_vccnz .LBB0_721
	s_andn2_b64 vcc, exec, s[44:45]
	s_cbranch_vccnz .LBB0_685
	s_barrier
	s_branch .LBB0_685
